# v69 + MLA unit prologue: second K/V tile loads issued without first draining the Q and first-tile loads
# speedup vs baseline: 1.0077x; 1.0013x over previous
; #define VM_WAIT() asm volatile("s_waitcnt vmcnt(0)" ::: "memory")
; #define A_SWRITE(bf) do { *(bf16x8*)(K_lds + (bf) * SHM_K + kws) = st_k0; *(bf16x8*)(K_lds + (bf) * SHM_K + kws + 32 * ROWB) = st_k1; \
;         if constexpr (DQK == 192) *(bf16x8*)(K_lds + (bf) * SHM_K + kws2) = st_k2; \
;         *(bf16x8*)(V_lds + (bf) * SHM_V + vst0) = st_v0; *(bf16x8*)(V_lds + (bf) * SHM_V + vst1) = st_v1; } while (0)
; #define A_BAR() do { asm volatile("s_waitcnt lgkmcnt(0)" ::: "memory"); __builtin_amdgcn_s_barrier(); asm volatile("" ::: "memory"); } while (0)
; template <int DQK, bool BIAS> ...
;     ...
;     m_reg = -1e30f; l_reg = 0.f;
; #pragma unroll
;     for (int d = 0; d < 4; ++d) o[d] = f32x16{};
;     A_SLOAD(kb0); VM_WAIT(); A_SWRITE(0);
;     if (NT > 1) { A_SLOAD(kb0 + 64); VM_WAIT(); A_SWRITE(1); }
;     __syncthreads();
;     if (wid >= 4) A_BAR();
; __device__ __forceinline__ void p4_mla_loop(Frame& F, const Args& A, const int qo) {
;     ...
;         const int it = __builtin_amdgcn_readfirstlane((int)F.MISC[16]);
;         if (it >= 512) break;
;         int ln = lane; asm volatile("" : "+v"(ln)); const int r32 = ln & 31, hi = ln >> 5;
;         const int qb = 31 - (it >> 4), bh = it & 15, b = bh >> 3, h = bh & 7;
;         const int m0 = b * SEQ + qb * 256 + wid * 32;
;         bf16x8 qr[12];
;         { const bf16_t* qp = WSP(bf16_t, WS_QF) + (size_t)(m0 + r32) * QFW + h * 192 + hi * 8;
; #pragma unroll
;           for (int d0 = 0; d0 < 12; ++d0) qr[d0] = *(const bf16x8*)(qp + d0 * 16); }
.LBB0_790:
	s_or_b64 exec, exec, s[4:5]
	s_waitcnt lgkmcnt(0)
	s_barrier
	ds_read_b32 v2, v191
	s_mov_b64 s[4:5], -1
	s_waitcnt lgkmcnt(0)
	v_readfirstlane_b32 s6, v2
	s_cmpk_lt_i32 s6, 0x200
	s_cbranch_scc0 .LBB0_785
	s_ashr_i32 s5, s6, 4
	s_lshl_b32 s4, s6, 10
	s_and_b32 s83, s6, 7
	s_and_b32 s8, s4, 0x2000
	s_lshl_b32 s4, s5, 8
	v_readlane_b32 s6, v254, 38
	s_sub_i32 s84, s6, s4
	v_mov_b32_e32 v200, v170
	s_addk_i32 s84, 0x1f00
	s_add_i32 s74, s84, s8
	v_and_b32_e32 v202, 31, v200
	v_or_b32_e32 v2, s74, v202
	v_mov_b64_e32 v[4:5], s[70:71]
	s_movk_i32 s6, 0xc00
	v_mad_i64_i32 v[4:5], s[6:7], v2, s6, v[4:5]
	s_lshl_b32 s6, s8, 12
	v_readlane_b32 s7, v255, 18
	s_add_u32 s6, s7, s6
	v_readlane_b32 s7, v255, 15
	v_ashrrev_i32_e32 v201, 5, v200
	s_addc_u32 s7, s7, 0
	s_lshl_b32 s9, s83, 9
	s_mul_i32 s68, s83, 0x180
	v_lshlrev_b32_e32 v6, 3, v201
	s_add_u32 s76, s6, s9
	v_lshl_add_u64 v[4:5], v[4:5], 0, s[68:69]
	v_ashrrev_i32_e32 v7, 31, v6
	s_addc_u32 s77, s7, 0
	s_lshl_b32 s6, s8, 7
	v_readlane_b32 s7, v255, 20
	v_lshl_add_u64 v[20:21], v[6:7], 1, v[4:5]
	s_add_u32 s6, s7, s6
	v_readlane_b32 s7, v255, 19
	v_lshl_add_u64 v[24:25], s[76:77], 0, v[174:175]
	global_load_dwordx4 v[154:157], v[20:21], off offset:32
	global_load_dwordx4 v[150:153], v[20:21], off offset:64
	global_load_dwordx4 v[142:145], v[20:21], off offset:96
	global_load_dwordx4 v[138:141], v[20:21], off offset:128
	global_load_dwordx4 v[134:137], v[20:21], off offset:160
	global_load_dwordx4 v[130:133], v[20:21], off offset:192
	global_load_dwordx4 v[126:129], v[20:21], off offset:224
	global_load_dwordx4 v[122:125], v[20:21], off offset:256
	global_load_dwordx4 v[118:121], v[20:21], off offset:288
	global_load_dwordx4 v[114:117], v[20:21], off offset:320
	s_addc_u32 s7, s7, 0
	v_add_co_u32_e32 v16, vcc, s96, v24
	v_lshl_add_u64 v[178:179], s[6:7], 0, v[176:177]
	s_nop 0
	v_addc_co_u32_e32 v17, vcc, 0, v25, vcc
	s_mov_b32 s6, 0x40000
	v_add_co_u32_e32 v36, vcc, s6, v24
	s_mov_b32 s6, 0x60000
	s_nop 0
	v_addc_co_u32_e32 v37, vcc, 0, v25, vcc
	global_load_dwordx4 v[4:7], v[16:17], off offset:256
	global_load_dwordx4 v[146:149], v[20:21], off offset:352
	global_load_dwordx4 v[8:11], v[24:25], off
	global_load_dwordx4 v[12:15], v[24:25], off offset:256
	s_nop 0
	global_load_dwordx4 v[16:19], v[16:17], off
	s_nop 0
	global_load_dwordx4 v[158:161], v[20:21], off
	s_nop 0
	global_load_dwordx4 v[20:23], v[178:179], off
	v_add_co_u32_e32 v40, vcc, s6, v24
	s_movk_i32 s6, 0x2000
	s_nop 0
	v_addc_co_u32_e32 v41, vcc, 0, v25, vcc
	v_add_co_u32_e32 v32, vcc, s6, v178
	global_load_dwordx4 v[24:27], v[36:37], off
	global_load_dwordx4 v[28:31], v[40:41], off
	v_addc_co_u32_e32 v33, vcc, 0, v179, vcc
	global_load_dwordx4 v[32:35], v[32:33], off
	s_nop 0
	global_load_dwordx4 v[36:39], v[36:37], off offset:256
	s_nop 0
	global_load_dwordx4 v[40:43], v[40:41], off offset:256
	v_readfirstlane_b32 s75, v0
	s_cmpk_lt_u32 s75, 0x100
	s_waitcnt vmcnt(9)
	ds_write_b128 v192, v[8:11] offset:49152
	s_waitcnt vmcnt(7)
	ds_write_b128 v192, v[16:19] offset:61440
	s_waitcnt vmcnt(5)
	ds_write_b128 v193, v[20:23] offset:49408
	ds_write_b128 v194, v[12:15]
	ds_write_b128 v195, v[4:7]
	s_waitcnt vmcnt(0)
	s_waitcnt vmcnt(4)
	ds_write_b128 v196, v[24:27]
	s_waitcnt vmcnt(3)
	ds_write_b128 v196, v[28:31] offset:12288
	s_waitcnt vmcnt(2)
	ds_write_b128 v197, v[32:35]
	s_waitcnt vmcnt(1)
	ds_write_b128 v194, v[36:39] offset:16384
	s_waitcnt vmcnt(0)
	ds_write_b128 v195, v[40:43] offset:16384
	s_waitcnt lgkmcnt(0)
	s_barrier
	s_cbranch_scc1 .LBB0_793
	s_waitcnt lgkmcnt(0)
	s_barrier
